# nt cache policy on the once-read f32 weight loads (conversion loops + adaLN), on top of v040
# speedup vs baseline: 1.0018x; 1.0013x over previous
.LBB0_19:
	v_add_co_u32_e64 v18, s[6:7], s25, v6
	v_add_co_u32_e32 v16, vcc, 0xfffd6000, v6
	s_nop 0
	v_addc_co_u32_e64 v19, s[6:7], -1, v7, s[6:7]
	v_add_co_u32_e64 v20, s[6:7], s26, v6
	v_addc_co_u32_e32 v17, vcc, -1, v7, vcc
	s_nop 0
	v_addc_co_u32_e64 v21, s[6:7], -1, v7, s[6:7]
	v_add_co_u32_e64 v22, s[6:7], s27, v6
	s_add_i32 s36, s3, s35
	s_nop 0
	v_addc_co_u32_e64 v23, s[6:7], -1, v7, s[6:7]
	v_add_co_u32_e64 v24, s[6:7], s30, v6
	s_add_i32 s37, s36, 0x14200
	s_nop 0
	v_addc_co_u32_e64 v25, s[6:7], -1, v7, s[6:7]
	v_add_co_u32_e64 v26, s[6:7], s31, v6
	s_add_i32 s38, s36, 0x15200
	s_nop 0
	v_addc_co_u32_e64 v27, s[6:7], -1, v7, s[6:7]
	v_add_co_u32_e64 v28, s[6:7], s33, v6
	s_add_i32 s39, s36, 0x16200
	s_nop 0
	v_addc_co_u32_e64 v29, s[6:7], -1, v7, s[6:7]
	global_load_dword v56, v[18:19], off nt
	global_load_dword v58, v[20:21], off nt
	global_load_dword v60, v[22:23], off nt
	global_load_dword v62, v[24:25], off nt
	global_load_dword v64, v[16:17], off nt
	global_load_dword v66, v[26:27], off nt
	global_load_dword v68, v[28:29], off nt
	global_load_dword v70, v[6:7], off nt
	s_add_i32 s6, s36, 0x12200
	s_add_i32 s7, s36, 0x13200
	s_add_i32 s40, s36, 0x12210
	s_add_i32 s41, s36, 0x13210
	s_add_i32 s42, s36, 0x14210
	s_add_i32 s43, s36, 0x15210
	s_add_i32 s36, s36, 0x16210
	v_mov_b32_e32 v15, s6
	v_mov_b32_e32 v20, s7
	v_mov_b32_e32 v24, s37
	v_mov_b32_e32 v28, s38
	v_mov_b32_e32 v48, s39
	v_mov_b32_e32 v32, s40
	v_mov_b32_e32 v36, s41
	v_mov_b32_e32 v40, s42
	v_mov_b32_e32 v44, s43
	v_mov_b32_e32 v52, s36
	ds_read_b128 v[16:19], v15
	ds_read_b128 v[20:23], v20
	ds_read_b128 v[24:27], v24
	ds_read_b128 v[28:31], v28
	ds_read_b128 v[32:35], v32
	ds_read_b128 v[36:39], v36
	ds_read_b128 v[40:43], v40
	ds_read_b128 v[44:47], v44
	ds_read_b128 v[48:51], v48
	ds_read_b128 v[52:55], v52
	s_waitcnt lgkmcnt(9)
	v_mov_b32_e32 v72, v16
	s_waitcnt lgkmcnt(8)
	v_mov_b32_e32 v73, v20
	v_mov_b32_e32 v20, v17
	v_mov_b32_e32 v16, v18
	v_mov_b32_e32 v17, v22
	v_mov_b32_e32 v22, v19
	s_waitcnt lgkmcnt(7)
	v_mov_b32_e32 v18, v24
	s_waitcnt lgkmcnt(6)
	v_mov_b32_e32 v19, v28
	v_mov_b32_e32 v28, v25
	v_mov_b32_e32 v24, v26
	v_mov_b32_e32 v25, v30
	v_mov_b32_e32 v30, v27
	s_waitcnt lgkmcnt(5)
	v_mov_b32_e32 v26, v32
	s_waitcnt lgkmcnt(4)
	v_mov_b32_e32 v27, v36
	v_mov_b32_e32 v36, v33
	v_mov_b32_e32 v32, v34
	v_mov_b32_e32 v33, v38
	v_mov_b32_e32 v38, v35
	s_waitcnt lgkmcnt(3)
	v_mov_b32_e32 v34, v40
	s_waitcnt lgkmcnt(2)
	v_mov_b32_e32 v35, v44
	v_mov_b32_e32 v44, v41
	v_mov_b32_e32 v40, v42
	v_mov_b32_e32 v41, v46
	s_add_i32 s35, s35, 32
	v_mov_b32_e32 v46, v43
	v_lshl_add_u64 v[6:7], v[6:7], 0, s[8:9]
	s_cmp_eq_u32 s35, 0
	s_waitcnt vmcnt(3)
	v_pk_fma_f32 v[8:9], v[64:65], v[72:73], v[8:9] op_sel_hi:[0,1,1]
	v_pk_fma_f32 v[10:11], v[64:65], v[18:19], v[10:11] op_sel_hi:[0,1,1]
	s_waitcnt lgkmcnt(1)
	v_fmac_f32_e32 v14, v64, v48
	v_pk_fma_f32 v[8:9], v[56:57], v[20:21], v[8:9] op_sel_hi:[0,1,1]
	v_pk_fma_f32 v[10:11], v[56:57], v[28:29], v[10:11] op_sel_hi:[0,1,1]
	v_fmac_f32_e32 v14, v56, v49
	v_pk_fma_f32 v[8:9], v[58:59], v[16:17], v[8:9] op_sel_hi:[0,1,1]
	v_pk_fma_f32 v[10:11], v[58:59], v[24:25], v[10:11] op_sel_hi:[0,1,1]
	v_fmac_f32_e32 v14, v58, v50
	v_pk_fma_f32 v[8:9], v[60:61], v[22:23], v[8:9] op_sel_hi:[0,1,1]
	v_pk_fma_f32 v[10:11], v[60:61], v[30:31], v[10:11] op_sel_hi:[0,1,1]
	v_fmac_f32_e32 v14, v60, v51
	v_pk_fma_f32 v[8:9], v[62:63], v[26:27], v[8:9] op_sel_hi:[0,1,1]
	v_pk_fma_f32 v[10:11], v[62:63], v[34:35], v[10:11] op_sel_hi:[0,1,1]
	s_waitcnt lgkmcnt(0)
	v_fmac_f32_e32 v14, v62, v52
	s_waitcnt vmcnt(2)
	v_pk_fma_f32 v[8:9], v[66:67], v[36:37], v[8:9] op_sel_hi:[0,1,1]
	v_pk_fma_f32 v[10:11], v[66:67], v[44:45], v[10:11] op_sel_hi:[0,1,1]
	v_fmac_f32_e32 v14, v66, v53
	s_waitcnt vmcnt(1)
	v_pk_fma_f32 v[8:9], v[68:69], v[32:33], v[8:9] op_sel_hi:[0,1,1]
	v_pk_fma_f32 v[10:11], v[68:69], v[40:41], v[10:11] op_sel_hi:[0,1,1]
	v_fmac_f32_e32 v14, v68, v54
	s_waitcnt vmcnt(0)
	v_pk_fma_f32 v[8:9], v[70:71], v[38:39], v[8:9] op_sel_hi:[0,1,1]
	v_pk_fma_f32 v[10:11], v[70:71], v[46:47], v[10:11] op_sel_hi:[0,1,1]
	v_fmac_f32_e32 v14, v70, v55
	s_cbranch_scc0 .LBB0_19
	ds_write2st64_b32 v3, v8, v9 offset1:1
	ds_write2st64_b32 v3, v10, v11 offset0:2 offset1:3
	ds_write_b32 v3, v14 offset:1024
	s_waitcnt lgkmcnt(0)
	s_barrier
	s_and_saveexec_b64 s[6:7], s[4:5]
	s_cbranch_execz .LBB0_17
	s_mul_i32 s35, s23, 0x1800
	s_add_i32 s35, s35, s22
	v_add_u32_e32 v6, s35, v4
	v_ashrrev_i32_e32 v7, 31, v6
	v_lshl_add_u64 v[6:7], v[6:7], 2, s[10:11]
	global_load_dword v20, v[6:7], off
	ds_read2st64_b32 v[6:7], v13 offset1:5
	ds_read2st64_b32 v[8:9], v13 offset0:10 offset1:15
	ds_read2st64_b32 v[10:11], v13 offset0:20 offset1:25
	ds_read2st64_b32 v[14:15], v13 offset0:30 offset1:35
	v_mad_u64_u32 v[16:17], s[36:37], s23, 5, v[2:3]
	v_mov_b64_e32 v[18:19], s[18:19]
	s_ashr_i32 s23, s22, 31
	v_mad_i64_i32 v[16:17], s[36:37], v16, s20, v[18:19]
	v_lshl_add_u64 v[16:17], s[22:23], 2, v[16:17]
	s_waitcnt vmcnt(0) lgkmcnt(3)
	v_add_f32_e32 v6, v20, v6
	v_add_f32_e32 v6, v6, v7
	s_waitcnt lgkmcnt(2)
	v_add_f32_e32 v6, v6, v8
	v_add_f32_e32 v6, v6, v9
	s_waitcnt lgkmcnt(1)
	v_add_f32_e32 v6, v6, v10
	v_add_f32_e32 v6, v6, v11
	s_waitcnt lgkmcnt(0)
	v_add_f32_e32 v6, v6, v14
	v_add_f32_e32 v8, v6, v15
	v_lshl_add_u64 v[6:7], v[4:5], 2, v[16:17]
	global_store_dword v[6:7], v8, off
	s_branch .LBB0_17

.LBB0_57:
	s_lshl_b32 s27, s8, 1
	s_lshl_b32 s30, s20, 1
	v_or_b32_e32 v21, s27, v1
	v_or_b32_e32 v31, s30, v6
	s_add_i32 s31, s27, 4
	s_add_i32 s41, s30, 4
	s_add_i32 s49, s27, 8
	s_add_i32 s50, s30, 8
	s_add_i32 s51, s27, 12
	s_add_i32 s52, s30, 12
	s_add_i32 s53, s27, 16
	s_add_i32 s54, s30, 16
	s_add_i32 s55, s27, 20
	s_add_i32 s56, s30, 20
	s_add_i32 s57, s27, 24
	s_add_i32 s58, s30, 24
	s_add_i32 s27, s27, 28
	s_add_i32 s30, s30, 28
	v_add_u32_e32 v33, s5, v21
	v_add_u32_e32 v4, s26, v31
	v_or_b32_e32 v35, s31, v1
	v_or_b32_e32 v37, s41, v6
	v_or_b32_e32 v39, s49, v1
	v_or_b32_e32 v41, s50, v6
	v_or_b32_e32 v43, s51, v1
	v_or_b32_e32 v47, s52, v6
	v_or_b32_e32 v49, s53, v1
	v_or_b32_e32 v51, s54, v6
	v_or_b32_e32 v53, s55, v1
	v_or_b32_e32 v88, s56, v6
	v_or_b32_e32 v89, s57, v1
	v_or_b32_e32 v90, s58, v6
	v_or_b32_e32 v91, s27, v1
	v_or_b32_e32 v92, s30, v6
	v_mad_i64_i32 v[4:5], s[30:31], v4, s44, v[2:3]
	v_mad_i64_i32 v[54:55], s[30:31], v33, s44, v[2:3]
	v_add_u32_e32 v33, s5, v35
	v_add_u32_e32 v56, s26, v37
	v_add_u32_e32 v66, s5, v39
	v_add_u32_e32 v64, s26, v41
	v_add_u32_e32 v70, s5, v43
	v_add_u32_e32 v68, s26, v47
	v_add_u32_e32 v74, s5, v49
	v_add_u32_e32 v72, s26, v51
	v_add_u32_e32 v78, s5, v53
	v_add_u32_e32 v76, s26, v88
	v_add_u32_e32 v82, s5, v89
	v_add_u32_e32 v80, s26, v90
	v_add_u32_e32 v86, s5, v91
	v_add_u32_e32 v84, s26, v92
	v_mad_i64_i32 v[56:57], s[30:31], v56, s44, v[2:3]
	v_mad_i64_i32 v[58:59], s[30:31], v33, s44, v[2:3]
	v_mad_i64_i32 v[64:65], s[30:31], v64, s44, v[2:3]
	v_mad_i64_i32 v[66:67], s[30:31], v66, s44, v[2:3]
	v_mad_i64_i32 v[68:69], s[30:31], v68, s44, v[2:3]
	v_mad_i64_i32 v[70:71], s[30:31], v70, s44, v[2:3]
	v_mad_i64_i32 v[72:73], s[30:31], v72, s44, v[2:3]
	v_mad_i64_i32 v[74:75], s[30:31], v74, s44, v[2:3]
	v_mad_i64_i32 v[76:77], s[30:31], v76, s44, v[2:3]
	v_mad_i64_i32 v[78:79], s[30:31], v78, s44, v[2:3]
	v_mad_i64_i32 v[80:81], s[30:31], v80, s44, v[2:3]
	v_mad_i64_i32 v[82:83], s[30:31], v82, s44, v[2:3]
	v_mad_i64_i32 v[84:85], s[30:31], v84, s44, v[2:3]
	v_mad_i64_i32 v[86:87], s[30:31], v86, s44, v[2:3]
	global_load_dword v33, v[4:5], off nt
	global_load_dword v93, v[54:55], off nt
	global_load_dword v94, v[56:57], off nt
	global_load_dword v95, v[58:59], off nt
	global_load_dword v96, v[64:65], off nt
	global_load_dword v97, v[66:67], off nt
	global_load_dword v98, v[68:69], off nt
	global_load_dword v99, v[70:71], off nt
	global_load_dword v100, v[72:73], off nt
	global_load_dword v101, v[74:75], off nt
	global_load_dword v102, v[76:77], off nt
	global_load_dword v103, v[78:79], off nt
	global_load_dword v104, v[80:81], off nt
	global_load_dword v105, v[82:83], off nt
	global_load_dword v106, v[84:85], off nt
	global_load_dword v107, v[86:87], off nt
	s_add_i32 s20, s20, 16
	s_add_i32 s8, s8, 16
	s_add_i32 s21, s21, -16
	v_mad_u64_u32 v[4:5], s[30:31], v31, s43, v[10:11]
	s_cmp_lg_u32 s21, 0
	v_mad_u64_u32 v[54:55], s[30:31], v21, s43, v[10:11]
	v_mad_u64_u32 v[56:57], s[30:31], v37, s43, v[10:11]
	v_mad_u64_u32 v[58:59], s[30:31], v35, s43, v[10:11]
	v_mad_u64_u32 v[64:65], s[30:31], v41, s43, v[10:11]
	v_mad_u64_u32 v[66:67], s[30:31], v39, s43, v[10:11]
	v_mad_u64_u32 v[68:69], s[30:31], v47, s43, v[10:11]
	v_mad_u64_u32 v[70:71], s[30:31], v43, s43, v[10:11]
	v_mad_u64_u32 v[72:73], s[30:31], v51, s43, v[10:11]
	v_mad_u64_u32 v[74:75], s[30:31], v49, s43, v[10:11]
	v_mad_u64_u32 v[76:77], s[30:31], v88, s43, v[10:11]
	v_mad_u64_u32 v[78:79], s[30:31], v53, s43, v[10:11]
	v_mad_u64_u32 v[80:81], s[30:31], v90, s43, v[10:11]
	v_mad_u64_u32 v[82:83], s[30:31], v89, s43, v[10:11]
	v_mad_u64_u32 v[84:85], s[30:31], v92, s43, v[10:11]
	v_mad_u64_u32 v[86:87], s[30:31], v91, s43, v[10:11]
	s_waitcnt vmcnt(15)
	ds_write_b32 v4, v33
	s_waitcnt vmcnt(14)
	ds_write_b32 v54, v93
	s_waitcnt vmcnt(13)
	ds_write_b32 v56, v94
	s_waitcnt vmcnt(12)
	ds_write_b32 v58, v95
	s_waitcnt vmcnt(11)
	ds_write_b32 v64, v96
	s_waitcnt vmcnt(10)
	ds_write_b32 v66, v97
	s_waitcnt vmcnt(9)
	ds_write_b32 v68, v98
	s_waitcnt vmcnt(8)
	ds_write_b32 v70, v99
	s_waitcnt vmcnt(7)
	ds_write_b32 v72, v100
	s_waitcnt vmcnt(6)
	ds_write_b32 v74, v101
	s_waitcnt vmcnt(5)
	ds_write_b32 v76, v102
	s_waitcnt vmcnt(4)
	ds_write_b32 v78, v103
	s_waitcnt vmcnt(3)
	ds_write_b32 v80, v104
	s_waitcnt vmcnt(2)
	ds_write_b32 v82, v105
	s_waitcnt vmcnt(1)
	ds_write_b32 v84, v106
	s_waitcnt vmcnt(0)
	ds_write_b32 v86, v107
	s_cbranch_scc1 .LBB0_57

.LBB0_141:
	s_lshl_b32 s38, s21, 1
	s_lshl_b32 s39, s31, 1
	v_or_b32_e32 v21, s38, v1
	v_or_b32_e32 v31, s39, v6
	s_add_i32 s40, s38, 4
	s_add_i32 s41, s39, 4
	s_add_i32 s49, s38, 8
	s_add_i32 s50, s39, 8
	s_add_i32 s51, s38, 12
	s_add_i32 s52, s39, 12
	s_add_i32 s53, s38, 16
	s_add_i32 s54, s39, 16
	s_add_i32 s55, s38, 20
	s_add_i32 s56, s39, 20
	s_add_i32 s57, s38, 24
	s_add_i32 s58, s39, 24
	s_add_i32 s38, s38, 28
	s_add_i32 s39, s39, 28
	v_add_u32_e32 v56, s34, v31
	v_or_b32_e32 v33, s40, v1
	v_or_b32_e32 v35, s41, v6
	v_or_b32_e32 v37, s49, v1
	v_or_b32_e32 v39, s50, v6
	v_or_b32_e32 v41, s51, v1
	v_or_b32_e32 v43, s52, v6
	v_or_b32_e32 v47, s53, v1
	v_or_b32_e32 v49, s54, v6
	v_or_b32_e32 v51, s55, v1
	v_or_b32_e32 v53, s56, v6
	v_or_b32_e32 v90, s57, v1
	v_or_b32_e32 v91, s58, v6
	v_or_b32_e32 v92, s38, v1
	v_or_b32_e32 v93, s39, v6
	v_add_u32_e32 v4, s20, v21
	v_ashrrev_i32_e32 v57, 31, v56
	v_add_u32_e32 v58, s20, v33
	v_add_u32_e32 v64, s34, v35
	v_add_u32_e32 v66, s20, v37
	v_add_u32_e32 v68, s34, v39
	v_add_u32_e32 v70, s20, v41
	v_add_u32_e32 v72, s34, v43
	v_add_u32_e32 v74, s20, v47
	v_add_u32_e32 v76, s34, v49
	v_add_u32_e32 v78, s20, v51
	v_add_u32_e32 v80, s34, v53
	v_add_u32_e32 v82, s20, v90
	v_add_u32_e32 v84, s34, v91
	v_add_u32_e32 v86, s20, v92
	v_add_u32_e32 v88, s34, v93
	v_ashrrev_i32_e32 v5, 31, v4
	v_lshlrev_b64 v[56:57], 12, v[56:57]
	v_ashrrev_i32_e32 v65, 31, v64
	v_ashrrev_i32_e32 v59, 31, v58
	v_ashrrev_i32_e32 v69, 31, v68
	v_ashrrev_i32_e32 v67, 31, v66
	v_ashrrev_i32_e32 v73, 31, v72
	v_ashrrev_i32_e32 v71, 31, v70
	v_ashrrev_i32_e32 v77, 31, v76
	v_ashrrev_i32_e32 v75, 31, v74
	v_ashrrev_i32_e32 v81, 31, v80
	v_ashrrev_i32_e32 v79, 31, v78
	v_ashrrev_i32_e32 v85, 31, v84
	v_ashrrev_i32_e32 v83, 31, v82
	v_ashrrev_i32_e32 v89, 31, v88
	v_ashrrev_i32_e32 v87, 31, v86
	v_lshlrev_b64 v[4:5], 12, v[4:5]
	v_lshl_add_u64 v[56:57], v[2:3], 0, v[56:57]
	v_lshlrev_b64 v[58:59], 12, v[58:59]
	v_lshlrev_b64 v[64:65], 12, v[64:65]
	v_lshlrev_b64 v[66:67], 12, v[66:67]
	v_lshlrev_b64 v[68:69], 12, v[68:69]
	v_lshlrev_b64 v[70:71], 12, v[70:71]
	v_lshlrev_b64 v[72:73], 12, v[72:73]
	v_lshlrev_b64 v[74:75], 12, v[74:75]
	v_lshlrev_b64 v[76:77], 12, v[76:77]
	v_lshlrev_b64 v[78:79], 12, v[78:79]
	v_lshlrev_b64 v[80:81], 12, v[80:81]
	v_lshlrev_b64 v[82:83], 12, v[82:83]
	v_lshlrev_b64 v[84:85], 12, v[84:85]
	v_lshlrev_b64 v[86:87], 12, v[86:87]
	v_lshlrev_b64 v[88:89], 12, v[88:89]
	v_lshl_add_u64 v[4:5], v[2:3], 0, v[4:5]
	v_lshl_add_u64 v[64:65], v[2:3], 0, v[64:65]
	v_lshl_add_u64 v[58:59], v[2:3], 0, v[58:59]
	v_lshl_add_u64 v[68:69], v[2:3], 0, v[68:69]
	v_lshl_add_u64 v[66:67], v[2:3], 0, v[66:67]
	v_lshl_add_u64 v[72:73], v[2:3], 0, v[72:73]
	v_lshl_add_u64 v[70:71], v[2:3], 0, v[70:71]
	v_lshl_add_u64 v[76:77], v[2:3], 0, v[76:77]
	v_lshl_add_u64 v[74:75], v[2:3], 0, v[74:75]
	v_lshl_add_u64 v[80:81], v[2:3], 0, v[80:81]
	v_lshl_add_u64 v[78:79], v[2:3], 0, v[78:79]
	v_lshl_add_u64 v[84:85], v[2:3], 0, v[84:85]
	v_lshl_add_u64 v[82:83], v[2:3], 0, v[82:83]
	v_lshl_add_u64 v[88:89], v[2:3], 0, v[88:89]
	v_lshl_add_u64 v[86:87], v[2:3], 0, v[86:87]
	global_load_dword v94, v[56:57], off nt
	global_load_dword v95, v[4:5], off nt
	global_load_dword v96, v[64:65], off nt
	global_load_dword v97, v[58:59], off nt
	global_load_dword v98, v[68:69], off nt
	global_load_dword v99, v[66:67], off nt
	global_load_dword v100, v[72:73], off nt
	global_load_dword v101, v[70:71], off nt
	global_load_dword v102, v[76:77], off nt
	global_load_dword v103, v[74:75], off nt
	global_load_dword v104, v[80:81], off nt
	global_load_dword v105, v[78:79], off nt
	global_load_dword v106, v[84:85], off nt
	global_load_dword v107, v[82:83], off nt
	global_load_dword v108, v[88:89], off nt
	global_load_dword v109, v[86:87], off nt
	s_add_i32 s31, s31, 16
	s_add_i32 s21, s21, 16
	s_add_i32 s35, s35, -16
	v_mad_u64_u32 v[4:5], s[38:39], v31, s43, v[10:11]
	s_cmp_lg_u32 s35, 0
	v_mad_u64_u32 v[56:57], s[38:39], v21, s43, v[10:11]
	v_mad_u64_u32 v[58:59], s[38:39], v35, s43, v[10:11]
	v_mad_u64_u32 v[64:65], s[38:39], v33, s43, v[10:11]
	v_mad_u64_u32 v[66:67], s[38:39], v39, s43, v[10:11]
	v_mad_u64_u32 v[68:69], s[38:39], v37, s43, v[10:11]
	v_mad_u64_u32 v[70:71], s[38:39], v43, s43, v[10:11]
	v_mad_u64_u32 v[72:73], s[38:39], v41, s43, v[10:11]
	v_mad_u64_u32 v[74:75], s[38:39], v49, s43, v[10:11]
	v_mad_u64_u32 v[76:77], s[38:39], v47, s43, v[10:11]
	v_mad_u64_u32 v[78:79], s[38:39], v53, s43, v[10:11]
	v_mad_u64_u32 v[80:81], s[38:39], v51, s43, v[10:11]
	v_mad_u64_u32 v[82:83], s[38:39], v91, s43, v[10:11]
	v_mad_u64_u32 v[84:85], s[38:39], v90, s43, v[10:11]
	v_mad_u64_u32 v[86:87], s[38:39], v93, s43, v[10:11]
	v_mad_u64_u32 v[88:89], s[38:39], v92, s43, v[10:11]
	s_waitcnt vmcnt(15)
	ds_write_b32 v4, v94
	s_waitcnt vmcnt(14)
	ds_write_b32 v56, v95
	s_waitcnt vmcnt(13)
	ds_write_b32 v58, v96
	s_waitcnt vmcnt(12)
	ds_write_b32 v64, v97
	s_waitcnt vmcnt(11)
	ds_write_b32 v66, v98
	s_waitcnt vmcnt(10)
	ds_write_b32 v68, v99
	s_waitcnt vmcnt(9)
	ds_write_b32 v70, v100
	s_waitcnt vmcnt(8)
	ds_write_b32 v72, v101
	s_waitcnt vmcnt(7)
	ds_write_b32 v74, v102
	s_waitcnt vmcnt(6)
	ds_write_b32 v76, v103
	s_waitcnt vmcnt(5)
	ds_write_b32 v78, v104
	s_waitcnt vmcnt(4)
	ds_write_b32 v80, v105
	s_waitcnt vmcnt(3)
	ds_write_b32 v82, v106
	s_waitcnt vmcnt(2)
	ds_write_b32 v84, v107
	s_waitcnt vmcnt(1)
	ds_write_b32 v86, v108
	s_waitcnt vmcnt(0)
	ds_write_b32 v88, v109
	s_cbranch_scc1 .LBB0_141

.LBB0_155:
	s_lshl_b32 s36, s21, 1
	s_lshl_b32 s37, s27, 1
	v_or_b32_e32 v21, s36, v1
	v_or_b32_e32 v31, s37, v6
	s_add_i32 s38, s36, 4
	s_add_i32 s39, s37, 4
	s_add_i32 s40, s36, 8
	s_add_i32 s41, s37, 8
	s_add_i32 s49, s36, 12
	s_add_i32 s50, s37, 12
	s_add_i32 s51, s36, 16
	s_add_i32 s52, s37, 16
	s_add_i32 s53, s36, 20
	s_add_i32 s54, s37, 20
	s_add_i32 s55, s36, 24
	s_add_i32 s56, s37, 24
	s_add_i32 s36, s36, 28
	s_add_i32 s37, s37, 28
	v_add_u32_e32 v56, s30, v31
	v_or_b32_e32 v33, s38, v1
	v_or_b32_e32 v35, s39, v6
	v_or_b32_e32 v37, s40, v1
	v_or_b32_e32 v39, s41, v6
	v_or_b32_e32 v41, s49, v1
	v_or_b32_e32 v43, s50, v6
	v_or_b32_e32 v47, s51, v1
	v_or_b32_e32 v49, s52, v6
	v_or_b32_e32 v51, s53, v1
	v_or_b32_e32 v53, s54, v6
	v_or_b32_e32 v90, s55, v1
	v_or_b32_e32 v91, s56, v6
	v_or_b32_e32 v92, s36, v1
	v_or_b32_e32 v93, s37, v6
	v_add_u32_e32 v4, s20, v21
	v_ashrrev_i32_e32 v57, 31, v56
	v_add_u32_e32 v58, s20, v33
	v_add_u32_e32 v64, s30, v35
	v_add_u32_e32 v66, s20, v37
	v_add_u32_e32 v68, s30, v39
	v_add_u32_e32 v70, s20, v41
	v_add_u32_e32 v72, s30, v43
	v_add_u32_e32 v74, s20, v47
	v_add_u32_e32 v76, s30, v49
	v_add_u32_e32 v78, s20, v51
	v_add_u32_e32 v80, s30, v53
	v_add_u32_e32 v82, s20, v90
	v_add_u32_e32 v84, s30, v91
	v_add_u32_e32 v86, s20, v92
	v_add_u32_e32 v88, s30, v93
	v_ashrrev_i32_e32 v5, 31, v4
	v_lshlrev_b64 v[56:57], 12, v[56:57]
	v_ashrrev_i32_e32 v65, 31, v64
	v_ashrrev_i32_e32 v59, 31, v58
	v_ashrrev_i32_e32 v69, 31, v68
	v_ashrrev_i32_e32 v67, 31, v66
	v_ashrrev_i32_e32 v73, 31, v72
	v_ashrrev_i32_e32 v71, 31, v70
	v_ashrrev_i32_e32 v77, 31, v76
	v_ashrrev_i32_e32 v75, 31, v74
	v_ashrrev_i32_e32 v81, 31, v80
	v_ashrrev_i32_e32 v79, 31, v78
	v_ashrrev_i32_e32 v85, 31, v84
	v_ashrrev_i32_e32 v83, 31, v82
	v_ashrrev_i32_e32 v89, 31, v88
	v_ashrrev_i32_e32 v87, 31, v86
	v_lshlrev_b64 v[4:5], 12, v[4:5]
	v_lshl_add_u64 v[56:57], v[2:3], 0, v[56:57]
	v_lshlrev_b64 v[58:59], 12, v[58:59]
	v_lshlrev_b64 v[64:65], 12, v[64:65]
	v_lshlrev_b64 v[66:67], 12, v[66:67]
	v_lshlrev_b64 v[68:69], 12, v[68:69]
	v_lshlrev_b64 v[70:71], 12, v[70:71]
	v_lshlrev_b64 v[72:73], 12, v[72:73]
	v_lshlrev_b64 v[74:75], 12, v[74:75]
	v_lshlrev_b64 v[76:77], 12, v[76:77]
	v_lshlrev_b64 v[78:79], 12, v[78:79]
	v_lshlrev_b64 v[80:81], 12, v[80:81]
	v_lshlrev_b64 v[82:83], 12, v[82:83]
	v_lshlrev_b64 v[84:85], 12, v[84:85]
	v_lshlrev_b64 v[86:87], 12, v[86:87]
	v_lshlrev_b64 v[88:89], 12, v[88:89]
	v_lshl_add_u64 v[4:5], v[2:3], 0, v[4:5]
	v_lshl_add_u64 v[64:65], v[2:3], 0, v[64:65]
	v_lshl_add_u64 v[58:59], v[2:3], 0, v[58:59]
	v_lshl_add_u64 v[68:69], v[2:3], 0, v[68:69]
	v_lshl_add_u64 v[66:67], v[2:3], 0, v[66:67]
	v_lshl_add_u64 v[72:73], v[2:3], 0, v[72:73]
	v_lshl_add_u64 v[70:71], v[2:3], 0, v[70:71]
	v_lshl_add_u64 v[76:77], v[2:3], 0, v[76:77]
	v_lshl_add_u64 v[74:75], v[2:3], 0, v[74:75]
	v_lshl_add_u64 v[80:81], v[2:3], 0, v[80:81]
	v_lshl_add_u64 v[78:79], v[2:3], 0, v[78:79]
	v_lshl_add_u64 v[84:85], v[2:3], 0, v[84:85]
	v_lshl_add_u64 v[82:83], v[2:3], 0, v[82:83]
	v_lshl_add_u64 v[88:89], v[2:3], 0, v[88:89]
	v_lshl_add_u64 v[86:87], v[2:3], 0, v[86:87]
	global_load_dword v94, v[56:57], off nt
	global_load_dword v95, v[4:5], off nt
	global_load_dword v96, v[64:65], off nt
	global_load_dword v97, v[58:59], off nt
	global_load_dword v98, v[68:69], off nt
	global_load_dword v99, v[66:67], off nt
	global_load_dword v100, v[72:73], off nt
	global_load_dword v101, v[70:71], off nt
	global_load_dword v102, v[76:77], off nt
	global_load_dword v103, v[74:75], off nt
	global_load_dword v104, v[80:81], off nt
	global_load_dword v105, v[78:79], off nt
	global_load_dword v106, v[84:85], off nt
	global_load_dword v107, v[82:83], off nt
	global_load_dword v108, v[88:89], off nt
	global_load_dword v109, v[86:87], off nt
	s_add_i32 s27, s27, 16
	s_add_i32 s21, s21, 16
	s_add_i32 s31, s31, -16
	v_mad_u64_u32 v[4:5], s[36:37], v31, s43, v[10:11]
	s_cmp_lg_u32 s31, 0
	v_mad_u64_u32 v[56:57], s[36:37], v21, s43, v[10:11]
	v_mad_u64_u32 v[58:59], s[36:37], v35, s43, v[10:11]
	v_mad_u64_u32 v[64:65], s[36:37], v33, s43, v[10:11]
	v_mad_u64_u32 v[66:67], s[36:37], v39, s43, v[10:11]
	v_mad_u64_u32 v[68:69], s[36:37], v37, s43, v[10:11]
	v_mad_u64_u32 v[70:71], s[36:37], v43, s43, v[10:11]
	v_mad_u64_u32 v[72:73], s[36:37], v41, s43, v[10:11]
	v_mad_u64_u32 v[74:75], s[36:37], v49, s43, v[10:11]
	v_mad_u64_u32 v[76:77], s[36:37], v47, s43, v[10:11]
	v_mad_u64_u32 v[78:79], s[36:37], v53, s43, v[10:11]
	v_mad_u64_u32 v[80:81], s[36:37], v51, s43, v[10:11]
	v_mad_u64_u32 v[82:83], s[36:37], v91, s43, v[10:11]
	v_mad_u64_u32 v[84:85], s[36:37], v90, s43, v[10:11]
	v_mad_u64_u32 v[86:87], s[36:37], v93, s43, v[10:11]
	v_mad_u64_u32 v[88:89], s[36:37], v92, s43, v[10:11]
	s_waitcnt vmcnt(15)
	ds_write_b32 v4, v94
	s_waitcnt vmcnt(14)
	ds_write_b32 v56, v95
	s_waitcnt vmcnt(13)
	ds_write_b32 v58, v96
	s_waitcnt vmcnt(12)
	ds_write_b32 v64, v97
	s_waitcnt vmcnt(11)
	ds_write_b32 v66, v98
	s_waitcnt vmcnt(10)
	ds_write_b32 v68, v99
	s_waitcnt vmcnt(9)
	ds_write_b32 v70, v100
	s_waitcnt vmcnt(8)
	ds_write_b32 v72, v101
	s_waitcnt vmcnt(7)
	ds_write_b32 v74, v102
	s_waitcnt vmcnt(6)
	ds_write_b32 v76, v103
	s_waitcnt vmcnt(5)
	ds_write_b32 v78, v104
	s_waitcnt vmcnt(4)
	ds_write_b32 v80, v105
	s_waitcnt vmcnt(3)
	ds_write_b32 v82, v106
	s_waitcnt vmcnt(2)
	ds_write_b32 v84, v107
	s_waitcnt vmcnt(1)
	ds_write_b32 v86, v108
	s_waitcnt vmcnt(0)
	ds_write_b32 v88, v109
	s_cbranch_scc1 .LBB0_155

.LBB0_169:
	s_lshl_b32 s31, s21, 1
	s_lshl_b32 s36, s23, 1
	v_or_b32_e32 v21, s31, v1
	v_or_b32_e32 v31, s36, v6
	s_add_i32 s37, s31, 4
	s_add_i32 s38, s36, 4
	s_add_i32 s39, s31, 8
	s_add_i32 s40, s36, 8
	s_add_i32 s41, s31, 12
	s_add_i32 s47, s36, 12
	s_add_i32 s48, s31, 16
	s_add_i32 s49, s36, 16
	s_add_i32 s50, s31, 20
	s_add_i32 s51, s36, 20
	s_add_i32 s52, s31, 24
	s_add_i32 s53, s36, 24
	s_add_i32 s31, s31, 28
	s_add_i32 s36, s36, 28
	v_add_u32_e32 v56, s30, v31
	v_or_b32_e32 v33, s37, v1
	v_or_b32_e32 v35, s38, v6
	v_or_b32_e32 v37, s39, v1
	v_or_b32_e32 v39, s40, v6
	v_or_b32_e32 v41, s41, v1
	v_or_b32_e32 v43, s47, v6
	v_or_b32_e32 v47, s48, v1
	v_or_b32_e32 v49, s49, v6
	v_or_b32_e32 v51, s50, v1
	v_or_b32_e32 v53, s51, v6
	v_or_b32_e32 v90, s52, v1
	v_or_b32_e32 v91, s53, v6
	v_or_b32_e32 v92, s31, v1
	v_or_b32_e32 v93, s36, v6
	v_add_u32_e32 v4, s20, v21
	v_ashrrev_i32_e32 v57, 31, v56
	v_add_u32_e32 v58, s20, v33
	v_add_u32_e32 v64, s30, v35
	v_add_u32_e32 v66, s20, v37
	v_add_u32_e32 v68, s30, v39
	v_add_u32_e32 v70, s20, v41
	v_add_u32_e32 v72, s30, v43
	v_add_u32_e32 v74, s20, v47
	v_add_u32_e32 v76, s30, v49
	v_add_u32_e32 v78, s20, v51
	v_add_u32_e32 v80, s30, v53
	v_add_u32_e32 v82, s20, v90
	v_add_u32_e32 v84, s30, v91
	v_add_u32_e32 v86, s20, v92
	v_add_u32_e32 v88, s30, v93
	v_ashrrev_i32_e32 v5, 31, v4
	v_lshlrev_b64 v[56:57], 12, v[56:57]
	v_ashrrev_i32_e32 v65, 31, v64
	v_ashrrev_i32_e32 v59, 31, v58
	v_ashrrev_i32_e32 v69, 31, v68
	v_ashrrev_i32_e32 v67, 31, v66
	v_ashrrev_i32_e32 v73, 31, v72
	v_ashrrev_i32_e32 v71, 31, v70
	v_ashrrev_i32_e32 v77, 31, v76
	v_ashrrev_i32_e32 v75, 31, v74
	v_ashrrev_i32_e32 v81, 31, v80
	v_ashrrev_i32_e32 v79, 31, v78
	v_ashrrev_i32_e32 v85, 31, v84
	v_ashrrev_i32_e32 v83, 31, v82
	v_ashrrev_i32_e32 v89, 31, v88
	v_ashrrev_i32_e32 v87, 31, v86
	v_lshlrev_b64 v[4:5], 12, v[4:5]
	v_lshl_add_u64 v[56:57], v[2:3], 0, v[56:57]
	v_lshlrev_b64 v[58:59], 12, v[58:59]
	v_lshlrev_b64 v[64:65], 12, v[64:65]
	v_lshlrev_b64 v[66:67], 12, v[66:67]
	v_lshlrev_b64 v[68:69], 12, v[68:69]
	v_lshlrev_b64 v[70:71], 12, v[70:71]
	v_lshlrev_b64 v[72:73], 12, v[72:73]
	v_lshlrev_b64 v[74:75], 12, v[74:75]
	v_lshlrev_b64 v[76:77], 12, v[76:77]
	v_lshlrev_b64 v[78:79], 12, v[78:79]
	v_lshlrev_b64 v[80:81], 12, v[80:81]
	v_lshlrev_b64 v[82:83], 12, v[82:83]
	v_lshlrev_b64 v[84:85], 12, v[84:85]
	v_lshlrev_b64 v[86:87], 12, v[86:87]
	v_lshlrev_b64 v[88:89], 12, v[88:89]
	v_lshl_add_u64 v[4:5], v[2:3], 0, v[4:5]
	v_lshl_add_u64 v[64:65], v[2:3], 0, v[64:65]
	v_lshl_add_u64 v[58:59], v[2:3], 0, v[58:59]
	v_lshl_add_u64 v[68:69], v[2:3], 0, v[68:69]
	v_lshl_add_u64 v[66:67], v[2:3], 0, v[66:67]
	v_lshl_add_u64 v[72:73], v[2:3], 0, v[72:73]
	v_lshl_add_u64 v[70:71], v[2:3], 0, v[70:71]
	v_lshl_add_u64 v[76:77], v[2:3], 0, v[76:77]
	v_lshl_add_u64 v[74:75], v[2:3], 0, v[74:75]
	v_lshl_add_u64 v[80:81], v[2:3], 0, v[80:81]
	v_lshl_add_u64 v[78:79], v[2:3], 0, v[78:79]
	v_lshl_add_u64 v[84:85], v[2:3], 0, v[84:85]
	v_lshl_add_u64 v[82:83], v[2:3], 0, v[82:83]
	v_lshl_add_u64 v[88:89], v[2:3], 0, v[88:89]
	v_lshl_add_u64 v[86:87], v[2:3], 0, v[86:87]
	global_load_dword v94, v[56:57], off nt
	global_load_dword v95, v[4:5], off nt
	global_load_dword v96, v[64:65], off nt
	global_load_dword v97, v[58:59], off nt
	global_load_dword v98, v[68:69], off nt
	global_load_dword v99, v[66:67], off nt
	global_load_dword v100, v[72:73], off nt
	global_load_dword v101, v[70:71], off nt
	global_load_dword v102, v[76:77], off nt
	global_load_dword v103, v[74:75], off nt
	global_load_dword v104, v[80:81], off nt
	global_load_dword v105, v[78:79], off nt
	global_load_dword v106, v[84:85], off nt
	global_load_dword v107, v[82:83], off nt
	global_load_dword v108, v[88:89], off nt
	global_load_dword v109, v[86:87], off nt
	s_add_i32 s23, s23, 16
	s_add_i32 s21, s21, 16
	s_add_i32 s27, s27, -16
	v_mad_u64_u32 v[4:5], s[36:37], v31, s43, v[10:11]
	s_cmp_lg_u32 s27, 0
	v_mad_u64_u32 v[56:57], s[36:37], v21, s43, v[10:11]
	v_mad_u64_u32 v[58:59], s[36:37], v35, s43, v[10:11]
	v_mad_u64_u32 v[64:65], s[36:37], v33, s43, v[10:11]
	v_mad_u64_u32 v[66:67], s[36:37], v39, s43, v[10:11]
	v_mad_u64_u32 v[68:69], s[36:37], v37, s43, v[10:11]
	v_mad_u64_u32 v[70:71], s[36:37], v43, s43, v[10:11]
	v_mad_u64_u32 v[72:73], s[36:37], v41, s43, v[10:11]
	v_mad_u64_u32 v[74:75], s[36:37], v49, s43, v[10:11]
	v_mad_u64_u32 v[76:77], s[36:37], v47, s43, v[10:11]
	v_mad_u64_u32 v[78:79], s[36:37], v53, s43, v[10:11]
	v_mad_u64_u32 v[80:81], s[36:37], v51, s43, v[10:11]
	v_mad_u64_u32 v[82:83], s[36:37], v91, s43, v[10:11]
	v_mad_u64_u32 v[84:85], s[36:37], v90, s43, v[10:11]
	v_mad_u64_u32 v[86:87], s[36:37], v93, s43, v[10:11]
	v_mad_u64_u32 v[88:89], s[36:37], v92, s43, v[10:11]
	s_waitcnt vmcnt(15)
	ds_write_b32 v4, v94
	s_waitcnt vmcnt(14)
	ds_write_b32 v56, v95
	s_waitcnt vmcnt(13)
	ds_write_b32 v58, v96
	s_waitcnt vmcnt(12)
	ds_write_b32 v64, v97
	s_waitcnt vmcnt(11)
	ds_write_b32 v66, v98
	s_waitcnt vmcnt(10)
	ds_write_b32 v68, v99
	s_waitcnt vmcnt(9)
	ds_write_b32 v70, v100
	s_waitcnt vmcnt(8)
	ds_write_b32 v72, v101
	s_waitcnt vmcnt(7)
	ds_write_b32 v74, v102
	s_waitcnt vmcnt(6)
	ds_write_b32 v76, v103
	s_waitcnt vmcnt(5)
	ds_write_b32 v78, v104
	s_waitcnt vmcnt(4)
	ds_write_b32 v80, v105
	s_waitcnt vmcnt(3)
	ds_write_b32 v82, v106
	s_waitcnt vmcnt(2)
	ds_write_b32 v84, v107
	s_waitcnt vmcnt(1)
	ds_write_b32 v86, v108
	s_waitcnt vmcnt(0)
	ds_write_b32 v88, v109
	s_cbranch_scc1 .LBB0_169

.LBB0_185:
	s_lshl_b32 s41, s27, 1
	s_lshl_b32 s42, s20, 1
	v_or_b32_e32 v25, s41, v1
	v_or_b32_e32 v27, s42, v6
	s_add_i32 s43, s41, 4
	s_add_i32 s44, s42, 4
	s_add_i32 s45, s41, 8
	s_add_i32 s46, s42, 8
	s_add_i32 s47, s41, 12
	s_add_i32 s48, s42, 12
	s_add_i32 s49, s41, 16
	s_add_i32 s50, s42, 16
	s_add_i32 s51, s41, 20
	s_add_i32 s52, s42, 20
	s_add_i32 s53, s41, 24
	s_add_i32 s54, s42, 24
	s_add_i32 s41, s41, 28
	s_add_i32 s42, s42, 28
	v_add_u32_e32 v29, s21, v25
	v_add_u32_e32 v4, s26, v27
	v_or_b32_e32 v64, s43, v1
	v_or_b32_e32 v65, s44, v6
	v_or_b32_e32 v66, s45, v1
	v_or_b32_e32 v67, s46, v6
	v_or_b32_e32 v68, s47, v1
	v_or_b32_e32 v69, s48, v6
	v_or_b32_e32 v70, s49, v1
	v_or_b32_e32 v71, s50, v6
	v_or_b32_e32 v72, s51, v1
	v_or_b32_e32 v73, s52, v6
	v_or_b32_e32 v74, s53, v1
	v_or_b32_e32 v75, s54, v6
	v_or_b32_e32 v76, s41, v1
	v_or_b32_e32 v77, s42, v6
	v_mad_i64_i32 v[4:5], s[42:43], v4, s36, v[2:3]
	v_mad_i64_i32 v[30:31], s[42:43], v29, s36, v[2:3]
	v_add_u32_e32 v29, s21, v64
	v_add_u32_e32 v32, s26, v65
	v_add_u32_e32 v42, s21, v66
	v_add_u32_e32 v40, s26, v67
	v_add_u32_e32 v46, s21, v68
	v_add_u32_e32 v44, s26, v69
	v_add_u32_e32 v50, s21, v70
	v_add_u32_e32 v48, s26, v71
	v_add_u32_e32 v54, s21, v72
	v_add_u32_e32 v52, s26, v73
	v_add_u32_e32 v58, s21, v74
	v_add_u32_e32 v56, s26, v75
	v_add_u32_e32 v62, s21, v76
	v_add_u32_e32 v60, s26, v77
	v_mad_i64_i32 v[32:33], s[42:43], v32, s36, v[2:3]
	v_mad_i64_i32 v[34:35], s[42:43], v29, s36, v[2:3]
	v_mad_i64_i32 v[40:41], s[42:43], v40, s36, v[2:3]
	v_mad_i64_i32 v[42:43], s[42:43], v42, s36, v[2:3]
	v_mad_i64_i32 v[44:45], s[42:43], v44, s36, v[2:3]
	v_mad_i64_i32 v[46:47], s[42:43], v46, s36, v[2:3]
	v_mad_i64_i32 v[48:49], s[42:43], v48, s36, v[2:3]
	v_mad_i64_i32 v[50:51], s[42:43], v50, s36, v[2:3]
	v_mad_i64_i32 v[52:53], s[42:43], v52, s36, v[2:3]
	v_mad_i64_i32 v[54:55], s[42:43], v54, s36, v[2:3]
	v_mad_i64_i32 v[56:57], s[42:43], v56, s36, v[2:3]
	v_mad_i64_i32 v[58:59], s[42:43], v58, s36, v[2:3]
	v_mad_i64_i32 v[60:61], s[42:43], v60, s36, v[2:3]
	v_mad_i64_i32 v[62:63], s[42:43], v62, s36, v[2:3]
	global_load_dword v29, v[4:5], off nt
	global_load_dword v78, v[30:31], off nt
	global_load_dword v79, v[32:33], off nt
	global_load_dword v80, v[34:35], off nt
	global_load_dword v81, v[40:41], off nt
	global_load_dword v82, v[42:43], off nt
	global_load_dword v83, v[44:45], off nt
	global_load_dword v84, v[46:47], off nt
	global_load_dword v85, v[48:49], off nt
	global_load_dword v86, v[50:51], off nt
	global_load_dword v87, v[52:53], off nt
	global_load_dword v88, v[54:55], off nt
	global_load_dword v89, v[56:57], off nt
	global_load_dword v90, v[58:59], off nt
	global_load_dword v91, v[60:61], off nt
	global_load_dword v92, v[62:63], off nt
	s_add_i32 s20, s20, 16
	s_add_i32 s27, s27, 16
	s_add_i32 s31, s31, -16
	v_mad_u64_u32 v[4:5], s[42:43], v27, s37, v[10:11]
	s_cmp_lg_u32 s31, 0
	v_mad_u64_u32 v[30:31], s[42:43], v25, s37, v[10:11]
	v_mad_u64_u32 v[32:33], s[42:43], v65, s37, v[10:11]
	v_mad_u64_u32 v[34:35], s[42:43], v64, s37, v[10:11]
	v_mad_u64_u32 v[40:41], s[42:43], v67, s37, v[10:11]
	v_mad_u64_u32 v[42:43], s[42:43], v66, s37, v[10:11]
	v_mad_u64_u32 v[44:45], s[42:43], v69, s37, v[10:11]
	v_mad_u64_u32 v[46:47], s[42:43], v68, s37, v[10:11]
	v_mad_u64_u32 v[48:49], s[42:43], v71, s37, v[10:11]
	v_mad_u64_u32 v[50:51], s[42:43], v70, s37, v[10:11]
	v_mad_u64_u32 v[52:53], s[42:43], v73, s37, v[10:11]
	v_mad_u64_u32 v[54:55], s[42:43], v72, s37, v[10:11]
	v_mad_u64_u32 v[56:57], s[42:43], v75, s37, v[10:11]
	v_mad_u64_u32 v[58:59], s[42:43], v74, s37, v[10:11]
	v_mad_u64_u32 v[60:61], s[42:43], v77, s37, v[10:11]
	v_mad_u64_u32 v[62:63], s[42:43], v76, s37, v[10:11]
	s_waitcnt vmcnt(15)
	ds_write_b32 v4, v29
	s_waitcnt vmcnt(14)
	ds_write_b32 v30, v78
	s_waitcnt vmcnt(13)
	ds_write_b32 v32, v79
	s_waitcnt vmcnt(12)
	ds_write_b32 v34, v80
	s_waitcnt vmcnt(11)
	ds_write_b32 v40, v81
	s_waitcnt vmcnt(10)
	ds_write_b32 v42, v82
	s_waitcnt vmcnt(9)
	ds_write_b32 v44, v83
	s_waitcnt vmcnt(8)
	ds_write_b32 v46, v84
	s_waitcnt vmcnt(7)
	ds_write_b32 v48, v85
	s_waitcnt vmcnt(6)
	ds_write_b32 v50, v86
	s_waitcnt vmcnt(5)
	ds_write_b32 v52, v87
	s_waitcnt vmcnt(4)
	ds_write_b32 v54, v88
	s_waitcnt vmcnt(3)
	ds_write_b32 v56, v89
	s_waitcnt vmcnt(2)
	ds_write_b32 v58, v90
	s_waitcnt vmcnt(1)
	ds_write_b32 v60, v91
	s_waitcnt vmcnt(0)
	ds_write_b32 v62, v92
	s_cbranch_scc1 .LBB0_185

.LBB0_199:
	s_lshl_b32 s38, s21, 1
	s_lshl_b32 s39, s25, 1
	v_or_b32_e32 v25, s38, v1
	v_or_b32_e32 v27, s39, v6
	s_add_i32 s40, s38, 4
	s_add_i32 s41, s39, 4
	s_add_i32 s42, s38, 8
	s_add_i32 s43, s39, 8
	s_add_i32 s44, s38, 12
	s_add_i32 s45, s39, 12
	s_add_i32 s46, s38, 16
	s_add_i32 s47, s39, 16
	s_add_i32 s48, s38, 20
	s_add_i32 s49, s39, 20
	s_add_i32 s50, s38, 24
	s_add_i32 s51, s39, 24
	s_add_i32 s38, s38, 28
	s_add_i32 s39, s39, 28
	v_add_u32_e32 v32, s24, v27
	v_or_b32_e32 v29, s40, v1
	v_or_b32_e32 v66, s41, v6
	v_or_b32_e32 v67, s42, v1
	v_or_b32_e32 v68, s43, v6
	v_or_b32_e32 v69, s44, v1
	v_or_b32_e32 v70, s45, v6
	v_or_b32_e32 v71, s46, v1
	v_or_b32_e32 v72, s47, v6
	v_or_b32_e32 v73, s48, v1
	v_or_b32_e32 v74, s49, v6
	v_or_b32_e32 v75, s50, v1
	v_or_b32_e32 v76, s51, v6
	v_or_b32_e32 v77, s38, v1
	v_or_b32_e32 v78, s39, v6
	v_add_u32_e32 v4, s20, v25
	v_ashrrev_i32_e32 v33, 31, v32
	v_add_u32_e32 v34, s20, v29
	v_add_u32_e32 v40, s24, v66
	v_add_u32_e32 v42, s20, v67
	v_add_u32_e32 v44, s24, v68
	v_add_u32_e32 v46, s20, v69
	v_add_u32_e32 v48, s24, v70
	v_add_u32_e32 v50, s20, v71
	v_add_u32_e32 v52, s24, v72
	v_add_u32_e32 v54, s20, v73
	v_add_u32_e32 v56, s24, v74
	v_add_u32_e32 v58, s20, v75
	v_add_u32_e32 v60, s24, v76
	v_add_u32_e32 v62, s20, v77
	v_add_u32_e32 v64, s24, v78
	v_ashrrev_i32_e32 v5, 31, v4
	v_lshlrev_b64 v[32:33], 12, v[32:33]
	v_ashrrev_i32_e32 v41, 31, v40
	v_ashrrev_i32_e32 v35, 31, v34
	v_ashrrev_i32_e32 v45, 31, v44
	v_ashrrev_i32_e32 v43, 31, v42
	v_ashrrev_i32_e32 v49, 31, v48
	v_ashrrev_i32_e32 v47, 31, v46
	v_ashrrev_i32_e32 v53, 31, v52
	v_ashrrev_i32_e32 v51, 31, v50
	v_ashrrev_i32_e32 v57, 31, v56
	v_ashrrev_i32_e32 v55, 31, v54
	v_ashrrev_i32_e32 v61, 31, v60
	v_ashrrev_i32_e32 v59, 31, v58
	v_ashrrev_i32_e32 v65, 31, v64
	v_ashrrev_i32_e32 v63, 31, v62
	v_lshlrev_b64 v[4:5], 12, v[4:5]
	v_lshl_add_u64 v[32:33], v[2:3], 0, v[32:33]
	v_lshlrev_b64 v[34:35], 12, v[34:35]
	v_lshlrev_b64 v[40:41], 12, v[40:41]
	v_lshlrev_b64 v[42:43], 12, v[42:43]
	v_lshlrev_b64 v[44:45], 12, v[44:45]
	v_lshlrev_b64 v[46:47], 12, v[46:47]
	v_lshlrev_b64 v[48:49], 12, v[48:49]
	v_lshlrev_b64 v[50:51], 12, v[50:51]
	v_lshlrev_b64 v[52:53], 12, v[52:53]
	v_lshlrev_b64 v[54:55], 12, v[54:55]
	v_lshlrev_b64 v[56:57], 12, v[56:57]
	v_lshlrev_b64 v[58:59], 12, v[58:59]
	v_lshlrev_b64 v[60:61], 12, v[60:61]
	v_lshlrev_b64 v[62:63], 12, v[62:63]
	v_lshlrev_b64 v[64:65], 12, v[64:65]
	v_lshl_add_u64 v[4:5], v[2:3], 0, v[4:5]
	v_lshl_add_u64 v[40:41], v[2:3], 0, v[40:41]
	v_lshl_add_u64 v[34:35], v[2:3], 0, v[34:35]
	v_lshl_add_u64 v[44:45], v[2:3], 0, v[44:45]
	v_lshl_add_u64 v[42:43], v[2:3], 0, v[42:43]
	v_lshl_add_u64 v[48:49], v[2:3], 0, v[48:49]
	v_lshl_add_u64 v[46:47], v[2:3], 0, v[46:47]
	v_lshl_add_u64 v[52:53], v[2:3], 0, v[52:53]
	v_lshl_add_u64 v[50:51], v[2:3], 0, v[50:51]
	v_lshl_add_u64 v[56:57], v[2:3], 0, v[56:57]
	v_lshl_add_u64 v[54:55], v[2:3], 0, v[54:55]
	v_lshl_add_u64 v[60:61], v[2:3], 0, v[60:61]
	v_lshl_add_u64 v[58:59], v[2:3], 0, v[58:59]
	v_lshl_add_u64 v[64:65], v[2:3], 0, v[64:65]
	v_lshl_add_u64 v[62:63], v[2:3], 0, v[62:63]
	global_load_dword v79, v[32:33], off nt
	global_load_dword v80, v[4:5], off nt
	global_load_dword v81, v[40:41], off nt
	global_load_dword v82, v[34:35], off nt
	global_load_dword v83, v[44:45], off nt
	global_load_dword v84, v[42:43], off nt
	global_load_dword v85, v[48:49], off nt
	global_load_dword v86, v[46:47], off nt
	global_load_dword v87, v[52:53], off nt
	global_load_dword v88, v[50:51], off nt
	global_load_dword v89, v[56:57], off nt
	global_load_dword v90, v[54:55], off nt
	global_load_dword v91, v[60:61], off nt
	global_load_dword v92, v[58:59], off nt
	global_load_dword v93, v[64:65], off nt
	global_load_dword v94, v[62:63], off nt
	s_add_i32 s25, s25, 16
	s_add_i32 s21, s21, 16
	s_add_i32 s31, s31, -16
	v_mad_u64_u32 v[4:5], s[38:39], v27, s37, v[10:11]
	s_cmp_lg_u32 s31, 0
	v_mad_u64_u32 v[32:33], s[38:39], v25, s37, v[10:11]
	v_mad_u64_u32 v[34:35], s[38:39], v66, s37, v[10:11]
	v_mad_u64_u32 v[40:41], s[38:39], v29, s37, v[10:11]
	v_mad_u64_u32 v[42:43], s[38:39], v68, s37, v[10:11]
	v_mad_u64_u32 v[44:45], s[38:39], v67, s37, v[10:11]
	v_mad_u64_u32 v[46:47], s[38:39], v70, s37, v[10:11]
	v_mad_u64_u32 v[48:49], s[38:39], v69, s37, v[10:11]
	v_mad_u64_u32 v[50:51], s[38:39], v72, s37, v[10:11]
	v_mad_u64_u32 v[52:53], s[38:39], v71, s37, v[10:11]
	v_mad_u64_u32 v[54:55], s[38:39], v74, s37, v[10:11]
	v_mad_u64_u32 v[56:57], s[38:39], v73, s37, v[10:11]
	v_mad_u64_u32 v[58:59], s[38:39], v76, s37, v[10:11]
	v_mad_u64_u32 v[60:61], s[38:39], v75, s37, v[10:11]
	v_mad_u64_u32 v[62:63], s[38:39], v78, s37, v[10:11]
	v_mad_u64_u32 v[64:65], s[38:39], v77, s37, v[10:11]
	s_waitcnt vmcnt(15)
	ds_write_b32 v4, v79
	s_waitcnt vmcnt(14)
	ds_write_b32 v32, v80
	s_waitcnt vmcnt(13)
	ds_write_b32 v34, v81
	s_waitcnt vmcnt(12)
	ds_write_b32 v40, v82
	s_waitcnt vmcnt(11)
	ds_write_b32 v42, v83
	s_waitcnt vmcnt(10)
	ds_write_b32 v44, v84
	s_waitcnt vmcnt(9)
	ds_write_b32 v46, v85
	s_waitcnt vmcnt(8)
	ds_write_b32 v48, v86
	s_waitcnt vmcnt(7)
	ds_write_b32 v50, v87
	s_waitcnt vmcnt(6)
	ds_write_b32 v52, v88
	s_waitcnt vmcnt(5)
	ds_write_b32 v54, v89
	s_waitcnt vmcnt(4)
	ds_write_b32 v56, v90
	s_waitcnt vmcnt(3)
	ds_write_b32 v58, v91
	s_waitcnt vmcnt(2)
	ds_write_b32 v60, v92
	s_waitcnt vmcnt(1)
	ds_write_b32 v62, v93
	s_waitcnt vmcnt(0)
	ds_write_b32 v64, v94
	s_cbranch_scc1 .LBB0_199

.LBB0_215:
	s_lshl_b32 s40, s38, 1
	s_lshl_b32 s41, s19, 1
	v_or_b32_e32 v11, s40, v1
	v_or_b32_e32 v64, s41, v6
	s_add_i32 s42, s40, 4
	s_add_i32 s43, s41, 4
	s_add_i32 s44, s40, 8
	s_add_i32 s45, s41, 8
	s_add_i32 s46, s40, 12
	s_add_i32 s47, s41, 12
	s_add_i32 s48, s40, 16
	s_add_i32 s49, s41, 16
	s_add_i32 s50, s40, 20
	s_add_i32 s51, s41, 20
	s_add_i32 s52, s40, 24
	s_add_i32 s53, s41, 24
	s_add_i32 s40, s40, 28
	s_add_i32 s41, s41, 28
	v_add_u32_e32 v4, s18, v64
	v_or_b32_e32 v65, s42, v1
	v_or_b32_e32 v66, s43, v6
	v_or_b32_e32 v67, s44, v1
	v_or_b32_e32 v68, s45, v6
	v_or_b32_e32 v69, s46, v1
	v_or_b32_e32 v70, s47, v6
	v_or_b32_e32 v71, s48, v1
	v_or_b32_e32 v72, s49, v6
	v_or_b32_e32 v73, s50, v1
	v_or_b32_e32 v74, s51, v6
	v_or_b32_e32 v75, s52, v1
	v_or_b32_e32 v76, s53, v6
	v_or_b32_e32 v77, s40, v1
	v_or_b32_e32 v78, s41, v6
	v_add_u32_e32 v30, s23, v11
	v_mad_i64_i32 v[4:5], s[40:41], v4, s30, v[2:3]
	v_add_u32_e32 v34, s23, v65
	v_add_u32_e32 v32, s18, v66
	v_add_u32_e32 v42, s23, v67
	v_add_u32_e32 v40, s18, v68
	v_add_u32_e32 v46, s23, v69
	v_add_u32_e32 v44, s18, v70
	v_add_u32_e32 v50, s23, v71
	v_add_u32_e32 v48, s18, v72
	v_add_u32_e32 v54, s23, v73
	v_add_u32_e32 v52, s18, v74
	v_add_u32_e32 v58, s23, v75
	v_add_u32_e32 v56, s18, v76
	v_add_u32_e32 v62, s23, v77
	v_add_u32_e32 v60, s18, v78
	v_mad_i64_i32 v[30:31], s[40:41], v30, s30, v[2:3]
	v_mad_i64_i32 v[32:33], s[40:41], v32, s30, v[2:3]
	v_mad_i64_i32 v[34:35], s[40:41], v34, s30, v[2:3]
	v_mad_i64_i32 v[40:41], s[40:41], v40, s30, v[2:3]
	v_mad_i64_i32 v[42:43], s[40:41], v42, s30, v[2:3]
	v_mad_i64_i32 v[44:45], s[40:41], v44, s30, v[2:3]
	v_mad_i64_i32 v[46:47], s[40:41], v46, s30, v[2:3]
	v_mad_i64_i32 v[48:49], s[40:41], v48, s30, v[2:3]
	v_mad_i64_i32 v[50:51], s[40:41], v50, s30, v[2:3]
	v_mad_i64_i32 v[52:53], s[40:41], v52, s30, v[2:3]
	v_mad_i64_i32 v[54:55], s[40:41], v54, s30, v[2:3]
	v_mad_i64_i32 v[56:57], s[40:41], v56, s30, v[2:3]
	v_mad_i64_i32 v[58:59], s[40:41], v58, s30, v[2:3]
	v_mad_i64_i32 v[60:61], s[40:41], v60, s30, v[2:3]
	v_mad_i64_i32 v[62:63], s[40:41], v62, s30, v[2:3]
	global_load_dword v79, v[4:5], off nt
	global_load_dword v80, v[30:31], off nt
	global_load_dword v81, v[32:33], off nt
	global_load_dword v82, v[34:35], off nt
	global_load_dword v83, v[40:41], off nt
	global_load_dword v84, v[42:43], off nt
	global_load_dword v85, v[44:45], off nt
	global_load_dword v86, v[46:47], off nt
	global_load_dword v87, v[48:49], off nt
	global_load_dword v88, v[50:51], off nt
	global_load_dword v89, v[52:53], off nt
	global_load_dword v90, v[54:55], off nt
	global_load_dword v91, v[56:57], off nt
	global_load_dword v92, v[58:59], off nt
	global_load_dword v93, v[60:61], off nt
	global_load_dword v94, v[62:63], off nt
	s_add_i32 s19, s19, 16
	s_add_i32 s38, s38, 16
	s_add_i32 s39, s39, -16
	v_mad_u64_u32 v[4:5], s[40:41], v64, s31, v[10:11]
	s_cmp_lg_u32 s39, 0
	v_mad_u64_u32 v[30:31], s[40:41], v11, s31, v[10:11]
	v_mad_u64_u32 v[32:33], s[40:41], v66, s31, v[10:11]
	v_mad_u64_u32 v[34:35], s[40:41], v65, s31, v[10:11]
	v_mad_u64_u32 v[40:41], s[40:41], v68, s31, v[10:11]
	v_mad_u64_u32 v[42:43], s[40:41], v67, s31, v[10:11]
	v_mad_u64_u32 v[44:45], s[40:41], v70, s31, v[10:11]
	v_mad_u64_u32 v[46:47], s[40:41], v69, s31, v[10:11]
	v_mad_u64_u32 v[48:49], s[40:41], v72, s31, v[10:11]
	v_mad_u64_u32 v[50:51], s[40:41], v71, s31, v[10:11]
	v_mad_u64_u32 v[52:53], s[40:41], v74, s31, v[10:11]
	v_mad_u64_u32 v[54:55], s[40:41], v73, s31, v[10:11]
	v_mad_u64_u32 v[56:57], s[40:41], v76, s31, v[10:11]
	v_mad_u64_u32 v[58:59], s[40:41], v75, s31, v[10:11]
	v_mad_u64_u32 v[60:61], s[40:41], v78, s31, v[10:11]
	v_mad_u64_u32 v[62:63], s[40:41], v77, s31, v[10:11]
	s_waitcnt vmcnt(15)
	ds_write_b32 v4, v79
	s_waitcnt vmcnt(14)
	ds_write_b32 v30, v80
	s_waitcnt vmcnt(13)
	ds_write_b32 v32, v81
	s_waitcnt vmcnt(12)
	ds_write_b32 v34, v82
	s_waitcnt vmcnt(11)
	ds_write_b32 v40, v83
	s_waitcnt vmcnt(10)
	ds_write_b32 v42, v84
	s_waitcnt vmcnt(9)
	ds_write_b32 v44, v85
	s_waitcnt vmcnt(8)
	ds_write_b32 v46, v86
	s_waitcnt vmcnt(7)
	ds_write_b32 v48, v87
	s_waitcnt vmcnt(6)
	ds_write_b32 v50, v88
	s_waitcnt vmcnt(5)
	ds_write_b32 v52, v89
	s_waitcnt vmcnt(4)
	ds_write_b32 v54, v90
	s_waitcnt vmcnt(3)
	ds_write_b32 v56, v91
	s_waitcnt vmcnt(2)
	ds_write_b32 v58, v92
	s_waitcnt vmcnt(1)
	ds_write_b32 v60, v93
	s_waitcnt vmcnt(0)
	ds_write_b32 v62, v94
	s_cbranch_scc1 .LBB0_215

.LBB0_229:
	s_lshl_b32 s36, s33, 1
	s_lshl_b32 s37, s34, 1
	v_or_b32_e32 v11, s36, v1
	v_or_b32_e32 v66, s37, v6
	s_add_i32 s38, s36, 4
	s_add_i32 s39, s37, 4
	s_add_i32 s40, s36, 8
	s_add_i32 s41, s37, 8
	s_add_i32 s42, s36, 12
	s_add_i32 s43, s37, 12
	s_add_i32 s44, s36, 16
	s_add_i32 s45, s37, 16
	s_add_i32 s46, s36, 20
	s_add_i32 s47, s37, 20
	s_add_i32 s48, s36, 24
	s_add_i32 s49, s37, 24
	s_add_i32 s36, s36, 28
	s_add_i32 s37, s37, 28
	v_add_u32_e32 v32, s16, v66
	v_or_b32_e32 v67, s38, v1
	v_or_b32_e32 v68, s39, v6
	v_or_b32_e32 v69, s40, v1
	v_or_b32_e32 v70, s41, v6
	v_or_b32_e32 v71, s42, v1
	v_or_b32_e32 v72, s43, v6
	v_or_b32_e32 v73, s44, v1
	v_or_b32_e32 v74, s45, v6
	v_or_b32_e32 v75, s46, v1
	v_or_b32_e32 v76, s47, v6
	v_or_b32_e32 v77, s48, v1
	v_or_b32_e32 v78, s49, v6
	v_or_b32_e32 v79, s36, v1
	v_or_b32_e32 v80, s37, v6
	v_add_u32_e32 v4, s23, v11
	v_ashrrev_i32_e32 v33, 31, v32
	v_add_u32_e32 v34, s23, v67
	v_add_u32_e32 v40, s16, v68
	v_add_u32_e32 v42, s23, v69
	v_add_u32_e32 v44, s16, v70
	v_add_u32_e32 v46, s23, v71
	v_add_u32_e32 v48, s16, v72
	v_add_u32_e32 v50, s23, v73
	v_add_u32_e32 v52, s16, v74
	v_add_u32_e32 v54, s23, v75
	v_add_u32_e32 v56, s16, v76
	v_add_u32_e32 v58, s23, v77
	v_add_u32_e32 v60, s16, v78
	v_add_u32_e32 v62, s23, v79
	v_add_u32_e32 v64, s16, v80
	v_ashrrev_i32_e32 v5, 31, v4
	v_lshlrev_b64 v[32:33], 12, v[32:33]
	v_ashrrev_i32_e32 v41, 31, v40
	v_ashrrev_i32_e32 v35, 31, v34
	v_ashrrev_i32_e32 v45, 31, v44
	v_ashrrev_i32_e32 v43, 31, v42
	v_ashrrev_i32_e32 v49, 31, v48
	v_ashrrev_i32_e32 v47, 31, v46
	v_ashrrev_i32_e32 v53, 31, v52
	v_ashrrev_i32_e32 v51, 31, v50
	v_ashrrev_i32_e32 v57, 31, v56
	v_ashrrev_i32_e32 v55, 31, v54
	v_ashrrev_i32_e32 v61, 31, v60
	v_ashrrev_i32_e32 v59, 31, v58
	v_ashrrev_i32_e32 v65, 31, v64
	v_ashrrev_i32_e32 v63, 31, v62
	v_lshlrev_b64 v[4:5], 12, v[4:5]
	v_lshl_add_u64 v[32:33], v[2:3], 0, v[32:33]
	v_lshlrev_b64 v[34:35], 12, v[34:35]
	v_lshlrev_b64 v[40:41], 12, v[40:41]
	v_lshlrev_b64 v[42:43], 12, v[42:43]
	v_lshlrev_b64 v[44:45], 12, v[44:45]
	v_lshlrev_b64 v[46:47], 12, v[46:47]
	v_lshlrev_b64 v[48:49], 12, v[48:49]
	v_lshlrev_b64 v[50:51], 12, v[50:51]
	v_lshlrev_b64 v[52:53], 12, v[52:53]
	v_lshlrev_b64 v[54:55], 12, v[54:55]
	v_lshlrev_b64 v[56:57], 12, v[56:57]
	v_lshlrev_b64 v[58:59], 12, v[58:59]
	v_lshlrev_b64 v[60:61], 12, v[60:61]
	v_lshlrev_b64 v[62:63], 12, v[62:63]
	v_lshlrev_b64 v[64:65], 12, v[64:65]
	v_lshl_add_u64 v[4:5], v[2:3], 0, v[4:5]
	v_lshl_add_u64 v[40:41], v[2:3], 0, v[40:41]
	v_lshl_add_u64 v[34:35], v[2:3], 0, v[34:35]
	v_lshl_add_u64 v[44:45], v[2:3], 0, v[44:45]
	v_lshl_add_u64 v[42:43], v[2:3], 0, v[42:43]
	v_lshl_add_u64 v[48:49], v[2:3], 0, v[48:49]
	v_lshl_add_u64 v[46:47], v[2:3], 0, v[46:47]
	v_lshl_add_u64 v[52:53], v[2:3], 0, v[52:53]
	v_lshl_add_u64 v[50:51], v[2:3], 0, v[50:51]
	v_lshl_add_u64 v[56:57], v[2:3], 0, v[56:57]
	v_lshl_add_u64 v[54:55], v[2:3], 0, v[54:55]
	v_lshl_add_u64 v[60:61], v[2:3], 0, v[60:61]
	v_lshl_add_u64 v[58:59], v[2:3], 0, v[58:59]
	v_lshl_add_u64 v[64:65], v[2:3], 0, v[64:65]
	v_lshl_add_u64 v[62:63], v[2:3], 0, v[62:63]
	global_load_dword v81, v[32:33], off nt
	global_load_dword v82, v[4:5], off nt
	global_load_dword v83, v[40:41], off nt
	global_load_dword v84, v[34:35], off nt
	global_load_dword v85, v[44:45], off nt
	global_load_dword v86, v[42:43], off nt
	global_load_dword v87, v[48:49], off nt
	global_load_dword v88, v[46:47], off nt
	global_load_dword v89, v[52:53], off nt
	global_load_dword v90, v[50:51], off nt
	global_load_dword v91, v[56:57], off nt
	global_load_dword v92, v[54:55], off nt
	global_load_dword v93, v[60:61], off nt
	global_load_dword v94, v[58:59], off nt
	global_load_dword v95, v[64:65], off nt
	global_load_dword v96, v[62:63], off nt
	s_add_i32 s34, s34, 16
	s_add_i32 s33, s33, 16
	s_add_i32 s35, s35, -16
	v_mad_u64_u32 v[4:5], s[36:37], v66, s31, v[10:11]
	s_cmp_lg_u32 s35, 0
	v_mad_u64_u32 v[32:33], s[36:37], v11, s31, v[10:11]
	v_mad_u64_u32 v[34:35], s[36:37], v68, s31, v[10:11]
	v_mad_u64_u32 v[40:41], s[36:37], v67, s31, v[10:11]
	v_mad_u64_u32 v[42:43], s[36:37], v70, s31, v[10:11]
	v_mad_u64_u32 v[44:45], s[36:37], v69, s31, v[10:11]
	v_mad_u64_u32 v[46:47], s[36:37], v72, s31, v[10:11]
	v_mad_u64_u32 v[48:49], s[36:37], v71, s31, v[10:11]
	v_mad_u64_u32 v[50:51], s[36:37], v74, s31, v[10:11]
	v_mad_u64_u32 v[52:53], s[36:37], v73, s31, v[10:11]
	v_mad_u64_u32 v[54:55], s[36:37], v76, s31, v[10:11]
	v_mad_u64_u32 v[56:57], s[36:37], v75, s31, v[10:11]
	v_mad_u64_u32 v[58:59], s[36:37], v78, s31, v[10:11]
	v_mad_u64_u32 v[60:61], s[36:37], v77, s31, v[10:11]
	v_mad_u64_u32 v[62:63], s[36:37], v80, s31, v[10:11]
	v_mad_u64_u32 v[64:65], s[36:37], v79, s31, v[10:11]
	s_waitcnt vmcnt(15)
	ds_write_b32 v4, v81
	s_waitcnt vmcnt(14)
	ds_write_b32 v32, v82
	s_waitcnt vmcnt(13)
	ds_write_b32 v34, v83
	s_waitcnt vmcnt(12)
	ds_write_b32 v40, v84
	s_waitcnt vmcnt(11)
	ds_write_b32 v42, v85
	s_waitcnt vmcnt(10)
	ds_write_b32 v44, v86
	s_waitcnt vmcnt(9)
	ds_write_b32 v46, v87
	s_waitcnt vmcnt(8)
	ds_write_b32 v48, v88
	s_waitcnt vmcnt(7)
	ds_write_b32 v50, v89
	s_waitcnt vmcnt(6)
	ds_write_b32 v52, v90
	s_waitcnt vmcnt(5)
	ds_write_b32 v54, v91
	s_waitcnt vmcnt(4)
	ds_write_b32 v56, v92
	s_waitcnt vmcnt(3)
	ds_write_b32 v58, v93
	s_waitcnt vmcnt(2)
	ds_write_b32 v60, v94
	s_waitcnt vmcnt(1)
	ds_write_b32 v62, v95
	s_waitcnt vmcnt(0)
	ds_write_b32 v64, v96
	s_cbranch_scc1 .LBB0_229

.LBB0_387:
	s_lshl_b32 s47, s25, 1
	s_lshl_b32 s48, s20, 1
	v_or_b32_e32 v11, s47, v1
	v_or_b32_e32 v29, s48, v8
	s_add_i32 s49, s47, 4
	s_add_i32 s50, s48, 4
	s_add_i32 s51, s47, 8
	s_add_i32 s52, s48, 8
	s_add_i32 s53, s47, 12
	s_add_i32 s54, s48, 12
	s_add_i32 s55, s47, 16
	s_add_i32 s60, s48, 16
	s_add_i32 s61, s47, 20
	s_add_i32 s62, s48, 20
	s_add_i32 s63, s47, 24
	s_add_i32 s64, s48, 24
	s_add_i32 s47, s47, 28
	s_add_i32 s48, s48, 28
	v_add_u32_e32 v6, s26, v29
	v_or_b32_e32 v60, s49, v1
	v_or_b32_e32 v61, s50, v8
	v_or_b32_e32 v62, s51, v1
	v_or_b32_e32 v63, s52, v8
	v_or_b32_e32 v64, s53, v1
	v_or_b32_e32 v65, s54, v8
	v_or_b32_e32 v66, s55, v1
	v_or_b32_e32 v67, s60, v8
	v_or_b32_e32 v68, s61, v1
	v_or_b32_e32 v69, s62, v8
	v_or_b32_e32 v70, s63, v1
	v_or_b32_e32 v71, s64, v8
	v_or_b32_e32 v72, s47, v1
	v_or_b32_e32 v73, s48, v8
	v_add_u32_e32 v30, s21, v11
	v_mad_i64_i32 v[6:7], s[48:49], v6, s31, v[4:5]
	v_add_u32_e32 v34, s21, v60
	v_add_u32_e32 v32, s26, v61
	v_add_u32_e32 v38, s21, v62
	v_add_u32_e32 v36, s26, v63
	v_add_u32_e32 v42, s21, v64
	v_add_u32_e32 v40, s26, v65
	v_add_u32_e32 v46, s21, v66
	v_add_u32_e32 v44, s26, v67
	v_add_u32_e32 v50, s21, v68
	v_add_u32_e32 v48, s26, v69
	v_add_u32_e32 v54, s21, v70
	v_add_u32_e32 v52, s26, v71
	v_add_u32_e32 v58, s21, v72
	v_add_u32_e32 v56, s26, v73
	v_mad_i64_i32 v[30:31], s[48:49], v30, s31, v[4:5]
	v_mad_i64_i32 v[32:33], s[48:49], v32, s31, v[4:5]
	v_mad_i64_i32 v[34:35], s[48:49], v34, s31, v[4:5]
	v_mad_i64_i32 v[36:37], s[48:49], v36, s31, v[4:5]
	v_mad_i64_i32 v[38:39], s[48:49], v38, s31, v[4:5]
	v_mad_i64_i32 v[40:41], s[48:49], v40, s31, v[4:5]
	v_mad_i64_i32 v[42:43], s[48:49], v42, s31, v[4:5]
	v_mad_i64_i32 v[44:45], s[48:49], v44, s31, v[4:5]
	v_mad_i64_i32 v[46:47], s[48:49], v46, s31, v[4:5]
	v_mad_i64_i32 v[48:49], s[48:49], v48, s31, v[4:5]
	v_mad_i64_i32 v[50:51], s[48:49], v50, s31, v[4:5]
	v_mad_i64_i32 v[52:53], s[48:49], v52, s31, v[4:5]
	v_mad_i64_i32 v[54:55], s[48:49], v54, s31, v[4:5]
	v_mad_i64_i32 v[56:57], s[48:49], v56, s31, v[4:5]
	v_mad_i64_i32 v[58:59], s[48:49], v58, s31, v[4:5]
	global_load_dword v74, v[6:7], off nt
	global_load_dword v75, v[30:31], off nt
	global_load_dword v76, v[32:33], off nt
	global_load_dword v77, v[34:35], off nt
	global_load_dword v78, v[36:37], off nt
	global_load_dword v79, v[38:39], off nt
	global_load_dword v80, v[40:41], off nt
	global_load_dword v81, v[42:43], off nt
	global_load_dword v82, v[44:45], off nt
	global_load_dword v83, v[46:47], off nt
	global_load_dword v84, v[48:49], off nt
	global_load_dword v85, v[50:51], off nt
	global_load_dword v86, v[52:53], off nt
	global_load_dword v87, v[54:55], off nt
	global_load_dword v88, v[56:57], off nt
	global_load_dword v89, v[58:59], off nt
	s_add_i32 s20, s20, 16
	s_add_i32 s25, s25, 16
	s_add_i32 s27, s27, -16
	v_mad_u64_u32 v[6:7], s[48:49], v29, s33, v[10:11]
	s_cmp_lg_u32 s27, 0
	v_mad_u64_u32 v[30:31], s[48:49], v11, s33, v[10:11]
	v_mad_u64_u32 v[32:33], s[48:49], v61, s33, v[10:11]
	v_mad_u64_u32 v[34:35], s[48:49], v60, s33, v[10:11]
	v_mad_u64_u32 v[36:37], s[48:49], v63, s33, v[10:11]
	v_mad_u64_u32 v[38:39], s[48:49], v62, s33, v[10:11]
	v_mad_u64_u32 v[40:41], s[48:49], v65, s33, v[10:11]
	v_mad_u64_u32 v[42:43], s[48:49], v64, s33, v[10:11]
	v_mad_u64_u32 v[44:45], s[48:49], v67, s33, v[10:11]
	v_mad_u64_u32 v[46:47], s[48:49], v66, s33, v[10:11]
	v_mad_u64_u32 v[48:49], s[48:49], v69, s33, v[10:11]
	v_mad_u64_u32 v[50:51], s[48:49], v68, s33, v[10:11]
	v_mad_u64_u32 v[52:53], s[48:49], v71, s33, v[10:11]
	v_mad_u64_u32 v[54:55], s[48:49], v70, s33, v[10:11]
	v_mad_u64_u32 v[56:57], s[48:49], v73, s33, v[10:11]
	v_mad_u64_u32 v[58:59], s[48:49], v72, s33, v[10:11]
	s_waitcnt vmcnt(0)
	ds_write_b32 v6, v74
	s_waitcnt vmcnt(14)
	ds_write_b32 v30, v75
	s_waitcnt vmcnt(13)
	ds_write_b32 v32, v76
	s_waitcnt vmcnt(12)
	ds_write_b32 v34, v77
	s_waitcnt vmcnt(11)
	ds_write_b32 v36, v78
	s_waitcnt vmcnt(10)
	ds_write_b32 v38, v79
	s_waitcnt vmcnt(9)
	ds_write_b32 v40, v80
	s_waitcnt vmcnt(8)
	ds_write_b32 v42, v81
	s_waitcnt vmcnt(7)
	ds_write_b32 v44, v82
	s_waitcnt vmcnt(6)
	ds_write_b32 v46, v83
	s_waitcnt vmcnt(5)
	ds_write_b32 v48, v84
	s_waitcnt vmcnt(4)
	ds_write_b32 v50, v85
	s_waitcnt vmcnt(3)
	ds_write_b32 v52, v86
	s_waitcnt vmcnt(2)
	ds_write_b32 v54, v87
	s_waitcnt vmcnt(1)
	ds_write_b32 v56, v88
	s_waitcnt vmcnt(0)
	ds_write_b32 v58, v89
	s_cbranch_scc1 .LBB0_387

.LBB0_401:
	s_lshl_b32 s42, s23, 1
	s_lshl_b32 s43, s27, 1
	v_or_b32_e32 v11, s42, v1
	v_or_b32_e32 v29, s43, v8
	s_add_i32 s44, s42, 4
	s_add_i32 s45, s43, 4
	s_add_i32 s46, s42, 8
	s_add_i32 s47, s43, 8
	s_add_i32 s48, s42, 12
	s_add_i32 s49, s43, 12
	s_add_i32 s50, s42, 16
	s_add_i32 s51, s43, 16
	s_add_i32 s52, s42, 20
	s_add_i32 s53, s43, 20
	s_add_i32 s54, s42, 24
	s_add_i32 s55, s43, 24
	s_add_i32 s42, s42, 28
	s_add_i32 s43, s43, 28
	v_add_u32_e32 v32, s22, v29
	v_or_b32_e32 v62, s44, v1
	v_or_b32_e32 v63, s45, v8
	v_or_b32_e32 v64, s46, v1
	v_or_b32_e32 v65, s47, v8
	v_or_b32_e32 v66, s48, v1
	v_or_b32_e32 v67, s49, v8
	v_or_b32_e32 v68, s50, v1
	v_or_b32_e32 v69, s51, v8
	v_or_b32_e32 v70, s52, v1
	v_or_b32_e32 v71, s53, v8
	v_or_b32_e32 v72, s54, v1
	v_or_b32_e32 v73, s55, v8
	v_or_b32_e32 v74, s42, v1
	v_or_b32_e32 v75, s43, v8
	v_add_u32_e32 v6, s21, v11
	v_ashrrev_i32_e32 v33, 31, v32
	v_add_u32_e32 v34, s21, v62
	v_add_u32_e32 v36, s22, v63
	v_add_u32_e32 v38, s21, v64
	v_add_u32_e32 v40, s22, v65
	v_add_u32_e32 v42, s21, v66
	v_add_u32_e32 v44, s22, v67
	v_add_u32_e32 v46, s21, v68
	v_add_u32_e32 v48, s22, v69
	v_add_u32_e32 v50, s21, v70
	v_add_u32_e32 v52, s22, v71
	v_add_u32_e32 v54, s21, v72
	v_add_u32_e32 v56, s22, v73
	v_add_u32_e32 v58, s21, v74
	v_add_u32_e32 v60, s22, v75
	v_ashrrev_i32_e32 v7, 31, v6
	v_lshlrev_b64 v[32:33], 12, v[32:33]
	v_ashrrev_i32_e32 v37, 31, v36
	v_ashrrev_i32_e32 v35, 31, v34
	v_ashrrev_i32_e32 v41, 31, v40
	v_ashrrev_i32_e32 v39, 31, v38
	v_ashrrev_i32_e32 v45, 31, v44
	v_ashrrev_i32_e32 v43, 31, v42
	v_ashrrev_i32_e32 v49, 31, v48
	v_ashrrev_i32_e32 v47, 31, v46
	v_ashrrev_i32_e32 v53, 31, v52
	v_ashrrev_i32_e32 v51, 31, v50
	v_ashrrev_i32_e32 v57, 31, v56
	v_ashrrev_i32_e32 v55, 31, v54
	v_ashrrev_i32_e32 v61, 31, v60
	v_ashrrev_i32_e32 v59, 31, v58
	v_lshlrev_b64 v[6:7], 12, v[6:7]
	v_lshl_add_u64 v[32:33], v[4:5], 0, v[32:33]
	v_lshlrev_b64 v[34:35], 12, v[34:35]
	v_lshlrev_b64 v[36:37], 12, v[36:37]
	v_lshlrev_b64 v[38:39], 12, v[38:39]
	v_lshlrev_b64 v[40:41], 12, v[40:41]
	v_lshlrev_b64 v[42:43], 12, v[42:43]
	v_lshlrev_b64 v[44:45], 12, v[44:45]
	v_lshlrev_b64 v[46:47], 12, v[46:47]
	v_lshlrev_b64 v[48:49], 12, v[48:49]
	v_lshlrev_b64 v[50:51], 12, v[50:51]
	v_lshlrev_b64 v[52:53], 12, v[52:53]
	v_lshlrev_b64 v[54:55], 12, v[54:55]
	v_lshlrev_b64 v[56:57], 12, v[56:57]
	v_lshlrev_b64 v[58:59], 12, v[58:59]
	v_lshlrev_b64 v[60:61], 12, v[60:61]
	v_lshl_add_u64 v[6:7], v[4:5], 0, v[6:7]
	v_lshl_add_u64 v[36:37], v[4:5], 0, v[36:37]
	v_lshl_add_u64 v[34:35], v[4:5], 0, v[34:35]
	v_lshl_add_u64 v[40:41], v[4:5], 0, v[40:41]
	v_lshl_add_u64 v[38:39], v[4:5], 0, v[38:39]
	v_lshl_add_u64 v[44:45], v[4:5], 0, v[44:45]
	v_lshl_add_u64 v[42:43], v[4:5], 0, v[42:43]
	v_lshl_add_u64 v[48:49], v[4:5], 0, v[48:49]
	v_lshl_add_u64 v[46:47], v[4:5], 0, v[46:47]
	v_lshl_add_u64 v[52:53], v[4:5], 0, v[52:53]
	v_lshl_add_u64 v[50:51], v[4:5], 0, v[50:51]
	v_lshl_add_u64 v[56:57], v[4:5], 0, v[56:57]
	v_lshl_add_u64 v[54:55], v[4:5], 0, v[54:55]
	v_lshl_add_u64 v[60:61], v[4:5], 0, v[60:61]
	v_lshl_add_u64 v[58:59], v[4:5], 0, v[58:59]
	global_load_dword v76, v[32:33], off nt
	global_load_dword v77, v[6:7], off nt
	global_load_dword v78, v[36:37], off nt
	global_load_dword v79, v[34:35], off nt
	global_load_dword v80, v[40:41], off nt
	global_load_dword v81, v[38:39], off nt
	global_load_dword v82, v[44:45], off nt
	global_load_dword v83, v[42:43], off nt
	global_load_dword v84, v[48:49], off nt
	global_load_dword v85, v[46:47], off nt
	global_load_dword v86, v[52:53], off nt
	global_load_dword v87, v[50:51], off nt
	global_load_dword v88, v[56:57], off nt
	global_load_dword v89, v[54:55], off nt
	global_load_dword v90, v[60:61], off nt
	global_load_dword v91, v[58:59], off nt
	s_add_i32 s27, s27, 16
	s_add_i32 s23, s23, 16
	s_add_i32 s41, s41, -16
	v_mad_u64_u32 v[6:7], s[42:43], v29, s33, v[10:11]
	s_cmp_lg_u32 s41, 0
	v_mad_u64_u32 v[32:33], s[42:43], v11, s33, v[10:11]
	v_mad_u64_u32 v[34:35], s[42:43], v63, s33, v[10:11]
	v_mad_u64_u32 v[36:37], s[42:43], v62, s33, v[10:11]
	v_mad_u64_u32 v[38:39], s[42:43], v65, s33, v[10:11]
	v_mad_u64_u32 v[40:41], s[42:43], v64, s33, v[10:11]
	v_mad_u64_u32 v[42:43], s[42:43], v67, s33, v[10:11]
	v_mad_u64_u32 v[44:45], s[42:43], v66, s33, v[10:11]
	v_mad_u64_u32 v[46:47], s[42:43], v69, s33, v[10:11]
	v_mad_u64_u32 v[48:49], s[42:43], v68, s33, v[10:11]
	v_mad_u64_u32 v[50:51], s[42:43], v71, s33, v[10:11]
	v_mad_u64_u32 v[52:53], s[42:43], v70, s33, v[10:11]
	v_mad_u64_u32 v[54:55], s[42:43], v73, s33, v[10:11]
	v_mad_u64_u32 v[56:57], s[42:43], v72, s33, v[10:11]
	v_mad_u64_u32 v[58:59], s[42:43], v75, s33, v[10:11]
	v_mad_u64_u32 v[60:61], s[42:43], v74, s33, v[10:11]
	s_waitcnt vmcnt(0)
	ds_write_b32 v6, v76
	s_waitcnt vmcnt(14)
	ds_write_b32 v32, v77
	s_waitcnt vmcnt(13)
	ds_write_b32 v34, v78
	s_waitcnt vmcnt(12)
	ds_write_b32 v36, v79
	s_waitcnt vmcnt(11)
	ds_write_b32 v38, v80
	s_waitcnt vmcnt(10)
	ds_write_b32 v40, v81
	s_waitcnt vmcnt(9)
	ds_write_b32 v42, v82
	s_waitcnt vmcnt(8)
	ds_write_b32 v44, v83
	s_waitcnt vmcnt(7)
	ds_write_b32 v46, v84
	s_waitcnt vmcnt(6)
	ds_write_b32 v48, v85
	s_waitcnt vmcnt(5)
	ds_write_b32 v50, v86
	s_waitcnt vmcnt(4)
	ds_write_b32 v52, v87
	s_waitcnt vmcnt(3)
	ds_write_b32 v54, v88
	s_waitcnt vmcnt(2)
	ds_write_b32 v56, v89
	s_waitcnt vmcnt(1)
	ds_write_b32 v58, v90
	s_waitcnt vmcnt(0)
	ds_write_b32 v60, v91
	s_cbranch_scc1 .LBB0_401
